# baseline (speedup 1.0000x reference)
.Lh_stage3:
	s_setprio 0
	s_mov_b32 s47, 3
	s_sub_i32 s59, s42, s43
	s_cmp_lt_i32 s59, 1
	s_cbranch_scc1 .Lh_epilogue
	s_bfm_b64 exec, s59, 0
	s_branch .Lh_loop_first
	s_nop 0
	s_nop 0
	s_nop 0
	s_nop 0
	s_nop 0
	s_nop 0
	s_nop 0
